# MoE-down-0: workgroups that ran the MoE-up-0 GEMM keep the expert table in LDS; only the former conversion workgroups rebuild it
# speedup vs baseline: 1.0026x; 1.0004x over previous
.LBB0_997:
	v_add_u32_e32 v160, s33, v135
	s_and_b64 vcc, exec, s[4:5]
	s_cbranch_vccz .LBB0_1116
	s_load_dwordx2 s[6:7], s[2:3], 0x130
	v_cmp_gt_i32_e32 vcc, 32, v160
	s_waitcnt vmcnt(0) lgkmcnt(0)
	s_barrier
	v_readlane_b32 s8, v243, 0
	s_nop 1
	s_cmp_lt_u32 s8, 0xe0
	s_cbranch_scc0 .Ltab7_build
	v_cmp_eq_u32_e32 vcc, 0, v160
	s_mov_b64 s[4:5], exec
	s_branch .LBB0_1002
.Ltab7_build:
	s_and_saveexec_b64 s[4:5], vcc
	s_cbranch_execz .LBB0_1000
	v_lshlrev_b32_e32 v0, 6, v160
	v_ashrrev_i32_e32 v1, 31, v0
	v_lshl_add_u64 v[0:1], v[0:1], 2, s[6:7]
	v_add_co_u32_e32 v0, vcc, 0x40000, v0
	s_nop 1
	v_addc_co_u32_e32 v1, vcc, 0, v1, vcc
	global_load_dword v0, v[0:1], off sc1
	v_lshl_add_u32 v1, v160, 2, 0
	v_add_u32_e32 v1, 0x20000, v1
	s_waitcnt vmcnt(0)
	ds_write_b32 v1, v0
